# P0-end tail site T0: idle non-adaLN workgroups convert 12800 more layer-0 MoE weight items (TRIM L0 28,28,20)
# baseline (speedup 1.0000x reference)
.LBB0_277:
	v_mul_lo_u32 v17, s37, v1
	v_mul_lo_u32 v18, s37, v8
	v_mul_lo_u32 v21, s37, v2
	v_mul_lo_u32 v23, s37, v4
	v_mul_lo_u32 v25, s37, v6
	v_mul_lo_u32 v20, s37, v3
	v_mul_lo_u32 v22, s37, v5
	v_mul_lo_u32 v24, s37, v7
	v_and_b32_e32 v18, 0xf8, v18
	v_cvt_f32_ubyte0_e32 v19, v17
	v_and_b32_e32 v17, 0xfe, v21
	v_and_b32_e32 v26, 0xfc, v23
	v_and_b32_e32 v27, 0xfe, v25
	s_add_i32 s37, s37, s80
	v_cvt_f32_ubyte0_e32 v21, v20
	v_cvt_f32_ubyte0_e32 v23, v22
	v_cvt_f32_ubyte0_e32 v25, v24
	v_cvt_f32_ubyte0_e32 v18, v18
	v_cvt_f32_ubyte0_e32 v20, v17
	v_cvt_f32_ubyte0_e32 v22, v26
	v_cvt_f32_ubyte0_e32 v24, v27
	v_pk_mul_f32 v[18:19], v[18:19], s[36:37] op_sel_hi:[1,0]
	v_pk_mul_f32 v[20:21], v[20:21], s[36:37] op_sel_hi:[1,0]
	v_pk_mul_f32 v[22:23], v[22:23], s[36:37] op_sel_hi:[1,0]
	v_pk_mul_f32 v[24:25], v[24:25], s[36:37] op_sel_hi:[1,0]
	v_pk_mul_f32 v[26:27], v[18:19], 0.5 op_sel_hi:[1,0]
	v_pk_mul_f32 v[28:29], v[20:21], 0.5 op_sel_hi:[1,0]
	v_pk_mul_f32 v[30:31], v[22:23], 0.5 op_sel_hi:[1,0]
	v_pk_mul_f32 v[32:33], v[24:25], 0.5 op_sel_hi:[1,0]
	v_fract_f32_e32 v34, v26
	v_fract_f32_e32 v35, v27
	v_fract_f32_e32 v36, v28
	v_fract_f32_e32 v37, v29
	v_fract_f32_e32 v38, v30
	v_fract_f32_e32 v39, v31
	v_fract_f32_e32 v40, v32
	v_fract_f32_e32 v41, v33
	v_pk_add_f32 v[34:35], v[34:35], v[34:35]
	v_cmp_neq_f32_e64 s[0:1], s33, v27
	v_pk_add_f32 v[36:37], v[36:37], v[36:37]
	v_cmp_neq_f32_e64 s[18:19], s33, v28
	v_cmp_neq_f32_e64 s[20:21], s33, v29
	v_pk_add_f32 v[28:29], v[38:39], v[38:39]
	v_cmp_neq_f32_e64 s[22:23], s33, v30
	v_cmp_neq_f32_e64 s[24:25], s33, v31
	v_pk_add_f32 v[30:31], v[40:41], v[40:41]
	v_cmp_neq_f32_e64 s[26:27], s33, v32
	v_cmp_neq_f32_e64 s[28:29], s33, v33
	v_cmp_neq_f32_e64 s[30:31], s33, v26
	v_cndmask_b32_e64 v26, 0, v35, s[0:1]
	v_cmp_lt_f32_e64 s[0:1], 1.0, v18
	v_cndmask_b32_e64 v17, 0, v34, s[30:31]
	v_cndmask_b32_e64 v32, 0, v36, s[18:19]
	v_cndmask_b32_e64 v33, 0, v37, s[20:21]
	v_cmp_lt_f32_e64 s[18:19], 1.0, v20
	v_cmp_lt_f32_e64 s[20:21], 1.0, v21
	v_cndmask_b32_e64 v34, 0, v28, s[22:23]
	v_cndmask_b32_e64 v35, 0, v29, s[24:25]
	v_cmp_lt_f32_e64 s[22:23], 1.0, v22
	v_cmp_lt_f32_e64 s[24:25], 1.0, v23
	v_cndmask_b32_e64 v36, 0, v30, s[26:27]
	v_cndmask_b32_e64 v37, 0, v31, s[28:29]
	v_cmp_lt_f32_e64 s[26:27], 1.0, v24
	v_cmp_lt_f32_e64 s[28:29], 1.0, v25
	v_cmp_lt_f32_e64 s[30:31], 1.0, v19
	v_cndmask_b32_e64 v29, v21, v33, s[20:21]
	v_cndmask_b32_e64 v28, v20, v32, s[18:19]
	v_cndmask_b32_e64 v27, v19, v26, s[30:31]
	v_cndmask_b32_e64 v26, v18, v17, s[0:1]
	v_cndmask_b32_e64 v31, v23, v35, s[24:25]
	v_cndmask_b32_e64 v30, v22, v34, s[22:23]
	v_cndmask_b32_e64 v33, v25, v37, s[28:29]
	v_cndmask_b32_e64 v32, v24, v36, s[26:27]
	v_add_f32_e32 v17, v26, v26
	v_add_f32_e32 v35, v27, v27
	v_add_f32_e32 v36, v28, v28
	v_add_f32_e32 v37, v29, v29
	v_add_f32_e32 v38, v30, v30
	v_add_f32_e32 v39, v31, v31
	v_add_f32_e32 v40, v32, v32
	v_add_f32_e32 v41, v33, v33
	v_rndne_f32_e32 v34, v17
	v_rndne_f32_e32 v35, v35
	v_rndne_f32_e32 v36, v36
	v_rndne_f32_e32 v37, v37
	v_rndne_f32_e32 v38, v38
	v_rndne_f32_e32 v39, v39
	v_rndne_f32_e32 v40, v40
	v_rndne_f32_e32 v41, v41
	v_pk_fma_f32 v[26:27], v[34:35], -0.5, v[26:27] op_sel_hi:[1,0,1]
	v_pk_fma_f32 v[28:29], v[36:37], -0.5, v[28:29] op_sel_hi:[1,0,1]
	v_pk_fma_f32 v[30:31], v[38:39], -0.5, v[30:31] op_sel_hi:[1,0,1]
	v_pk_fma_f32 v[32:33], v[40:41], -0.5, v[32:33] op_sel_hi:[1,0,1]
	v_cvt_i32_f32_e32 v17, v35
	v_cvt_i32_f32_e32 v66, v34
	v_cvt_i32_f32_e32 v67, v37
	v_cvt_i32_f32_e32 v68, v36
	v_cvt_i32_f32_e32 v69, v39
	v_cvt_i32_f32_e32 v70, v38
	v_cvt_i32_f32_e32 v71, v41
	v_cvt_i32_f32_e32 v72, v40
	v_pk_mul_f32 v[34:35], v[26:27], v[26:27]
	v_pk_mul_f32 v[36:37], v[28:29], v[28:29]
	v_pk_mul_f32 v[38:39], v[30:31], v[30:31]
	v_pk_mul_f32 v[40:41], v[32:33], v[32:33]
	v_pk_fma_f32 v[42:43], v[34:35], s[38:39], v[12:13] op_sel_hi:[1,0,0]
	v_pk_fma_f32 v[46:47], v[34:35], s[46:47], v[14:15] op_sel_hi:[1,0,0]
	v_pk_fma_f32 v[48:49], v[36:37], s[38:39], v[12:13] op_sel_hi:[1,0,0]
	v_pk_fma_f32 v[52:53], v[36:37], s[46:47], v[14:15] op_sel_hi:[1,0,0]
	v_pk_fma_f32 v[54:55], v[38:39], s[38:39], v[12:13] op_sel_hi:[1,0,0]
	v_pk_fma_f32 v[58:59], v[38:39], s[46:47], v[14:15] op_sel_hi:[1,0,0]
	v_pk_fma_f32 v[60:61], v[40:41], s[38:39], v[12:13] op_sel_hi:[1,0,0]
	v_pk_fma_f32 v[64:65], v[40:41], s[46:47], v[14:15] op_sel_hi:[1,0,0]
	v_pk_fma_f32 v[42:43], v[34:35], v[42:43], s[40:41] op_sel_hi:[1,1,0]
	v_pk_fma_f32 v[46:47], v[34:35], v[46:47], s[48:49] op_sel_hi:[1,1,0]
	v_pk_fma_f32 v[48:49], v[36:37], v[48:49], s[40:41] op_sel_hi:[1,1,0]
	v_pk_fma_f32 v[52:53], v[36:37], v[52:53], s[48:49] op_sel_hi:[1,1,0]
	v_pk_fma_f32 v[54:55], v[38:39], v[54:55], s[40:41] op_sel_hi:[1,1,0]
	v_pk_fma_f32 v[58:59], v[38:39], v[58:59], s[48:49] op_sel_hi:[1,1,0]
	v_pk_fma_f32 v[60:61], v[40:41], v[60:61], s[40:41] op_sel_hi:[1,1,0]
	v_pk_fma_f32 v[64:65], v[40:41], v[64:65], s[48:49] op_sel_hi:[1,1,0]
	v_pk_mul_f32 v[44:45], v[26:27], v[34:35]
	v_pk_mul_f32 v[50:51], v[28:29], v[36:37]
	v_pk_mul_f32 v[56:57], v[30:31], v[38:39]
	v_pk_mul_f32 v[62:63], v[32:33], v[40:41]
	v_pk_fma_f32 v[42:43], v[34:35], v[42:43], s[42:43] op_sel_hi:[1,1,0]
	v_pk_fma_f32 v[46:47], v[34:35], v[46:47], s[50:51] op_sel_hi:[1,1,0]
	v_pk_fma_f32 v[48:49], v[36:37], v[48:49], s[42:43] op_sel_hi:[1,1,0]
	v_pk_fma_f32 v[52:53], v[36:37], v[52:53], s[50:51] op_sel_hi:[1,1,0]
	v_pk_fma_f32 v[54:55], v[38:39], v[54:55], s[42:43] op_sel_hi:[1,1,0]
	v_pk_fma_f32 v[58:59], v[38:39], v[58:59], s[50:51] op_sel_hi:[1,1,0]
	v_pk_fma_f32 v[60:61], v[40:41], v[60:61], s[42:43] op_sel_hi:[1,1,0]
	v_pk_fma_f32 v[64:65], v[40:41], v[64:65], s[50:51] op_sel_hi:[1,1,0]
	v_lshlrev_b32_e32 v73, 30, v17
	v_lshlrev_b32_e32 v74, 30, v66
	v_and_b32_e32 v17, 1, v17
	v_and_b32_e32 v66, 1, v66
	v_lshlrev_b32_e32 v76, 30, v67
	v_lshlrev_b32_e32 v77, 30, v68
	v_and_b32_e32 v67, 1, v67
	v_and_b32_e32 v68, 1, v68
	v_lshlrev_b32_e32 v78, 30, v69
	v_lshlrev_b32_e32 v79, 30, v70
	v_and_b32_e32 v69, 1, v69
	v_and_b32_e32 v70, 1, v70
	v_lshlrev_b32_e32 v80, 30, v71
	v_lshlrev_b32_e32 v81, 30, v72
	v_and_b32_e32 v71, 1, v71
	v_and_b32_e32 v72, 1, v72
	v_pk_mul_f32 v[42:43], v[44:45], v[42:43]
	v_pk_fma_f32 v[44:45], v[34:35], v[46:47], s[52:53] op_sel_hi:[1,1,0]
	v_pk_mul_f32 v[46:47], v[50:51], v[48:49]
	v_pk_fma_f32 v[48:49], v[36:37], v[52:53], s[52:53] op_sel_hi:[1,1,0]
	v_pk_mul_f32 v[50:51], v[56:57], v[54:55]
	v_pk_fma_f32 v[52:53], v[38:39], v[58:59], s[52:53] op_sel_hi:[1,1,0]
	v_pk_mul_f32 v[54:55], v[62:63], v[60:61]
	v_pk_fma_f32 v[56:57], v[40:41], v[64:65], s[52:53] op_sel_hi:[1,1,0]
	v_pk_fma_f32 v[26:27], v[26:27], s[44:45], v[42:43] op_sel_hi:[1,0,1]
	v_pk_fma_f32 v[34:35], v[34:35], v[44:45], 1.0 op_sel_hi:[1,1,0]
	v_cmp_eq_u32_e64 s[0:1], 0, v66
	v_pk_fma_f32 v[28:29], v[28:29], s[44:45], v[46:47] op_sel_hi:[1,0,1]
	v_pk_fma_f32 v[36:37], v[36:37], v[48:49], 1.0 op_sel_hi:[1,1,0]
	v_cmp_eq_u32_e64 s[18:19], 0, v68
	v_cmp_eq_u32_e64 s[20:21], 0, v67
	v_pk_fma_f32 v[30:31], v[30:31], s[44:45], v[50:51] op_sel_hi:[1,0,1]
	v_pk_fma_f32 v[38:39], v[38:39], v[52:53], 1.0 op_sel_hi:[1,1,0]
	v_cmp_eq_u32_e64 s[22:23], 0, v70
	v_cmp_eq_u32_e64 s[24:25], 0, v69
	v_pk_fma_f32 v[32:33], v[32:33], s[44:45], v[54:55] op_sel_hi:[1,0,1]
	v_pk_fma_f32 v[40:41], v[40:41], v[56:57], 1.0 op_sel_hi:[1,1,0]
	v_cmp_eq_u32_e64 s[26:27], 0, v72
	v_cmp_eq_u32_e64 s[28:29], 0, v71
	v_cmp_eq_u32_e64 s[30:31], 0, v17
	v_and_b32_e32 v73, 0x80000000, v73
	v_and_b32_e32 v74, 0x80000000, v74
	v_and_b32_e32 v76, 0x80000000, v76
	v_and_b32_e32 v77, 0x80000000, v77
	v_and_b32_e32 v58, 0x80000000, v78
	v_and_b32_e32 v59, 0x80000000, v79
	v_and_b32_e32 v60, 0x80000000, v80
	v_and_b32_e32 v61, 0x80000000, v81
	v_cndmask_b32_e64 v17, v35, v27, s[30:31]
	v_cndmask_b32_e64 v42, v34, v26, s[0:1]
	v_cndmask_b32_e64 v27, -v27, v35, s[30:31]
	v_cndmask_b32_e64 v26, -v26, v34, s[0:1]
	v_cndmask_b32_e64 v34, v37, v29, s[20:21]
	v_cndmask_b32_e64 v35, v36, v28, s[18:19]
	v_cndmask_b32_e64 v29, -v29, v37, s[20:21]
	v_cndmask_b32_e64 v28, -v28, v36, s[18:19]
	v_cndmask_b32_e64 v36, v39, v31, s[24:25]
	v_cndmask_b32_e64 v37, v38, v30, s[22:23]
	v_cndmask_b32_e64 v31, -v31, v39, s[24:25]
	v_cndmask_b32_e64 v30, -v30, v38, s[22:23]
	v_cndmask_b32_e64 v38, v41, v33, s[28:29]
	v_cndmask_b32_e64 v39, v40, v32, s[26:27]
	v_cndmask_b32_e64 v33, -v33, v41, s[28:29]
	v_cndmask_b32_e64 v32, -v32, v40, s[26:27]
	v_xor_b32_e32 v17, v73, v17
	v_xor_b32_e32 v40, v74, v42
	v_xor_b32_e32 v27, v73, v27
	v_xor_b32_e32 v26, v74, v26
	v_cmp_lg_f32_e64 s[0:1], s33, v19
	v_xor_b32_e32 v19, v76, v34
	v_xor_b32_e32 v34, v77, v35
	v_xor_b32_e32 v29, v76, v29
	v_xor_b32_e32 v28, v77, v28
	v_cmp_lg_f32_e64 s[18:19], s33, v21
	v_cmp_lg_f32_e64 s[20:21], s33, v20
	v_xor_b32_e32 v20, v58, v36
	v_xor_b32_e32 v21, v59, v37
	v_xor_b32_e32 v31, v58, v31
	v_xor_b32_e32 v30, v59, v30
	v_cmp_lg_f32_e64 s[22:23], s33, v23
	v_cmp_lg_f32_e64 s[24:25], s33, v22
	v_xor_b32_e32 v22, v60, v38
	v_xor_b32_e32 v23, v61, v39
	v_xor_b32_e32 v33, v60, v33
	v_xor_b32_e32 v32, v61, v32
	v_cmp_lg_f32_e64 s[26:27], s33, v25
	v_cmp_lg_f32_e64 s[28:29], s33, v24
	v_cmp_lg_f32_e64 s[30:31], s33, v18
	v_cndmask_b32_e64 v24, v9, v27, s[0:1]
	v_cndmask_b32_e64 v17, v16, -v17, s[0:1]
	v_cndmask_b32_e64 v18, v9, v26, s[30:31]
	v_cndmask_b32_e64 v25, v16, -v40, s[30:31]
	v_cndmask_b32_e64 v26, v9, v28, s[20:21]
	v_cndmask_b32_e64 v27, v9, v29, s[18:19]
	v_cndmask_b32_e64 v28, v16, -v34, s[20:21]
	v_cndmask_b32_e64 v29, v16, -v19, s[18:19]
	v_cndmask_b32_e64 v30, v9, v30, s[24:25]
	v_cndmask_b32_e64 v31, v9, v31, s[22:23]
	v_cndmask_b32_e64 v34, v16, -v21, s[24:25]
	v_cndmask_b32_e64 v35, v16, -v20, s[22:23]
	v_cndmask_b32_e64 v32, v9, v32, s[28:29]
	v_cndmask_b32_e64 v33, v9, v33, s[26:27]
	v_cndmask_b32_e64 v36, v16, -v23, s[28:29]
	v_cndmask_b32_e64 v37, v16, -v22, s[26:27]
	v_cndmask_b32_e64 v19, v17, v24, s[4:5]
	v_cndmask_b32_e32 v18, v25, v18, vcc
	v_cndmask_b32_e64 v21, v29, v27, s[6:7]
	v_cndmask_b32_e64 v20, v28, v26, s[8:9]
	v_cndmask_b32_e64 v23, v35, v31, s[10:11]
	v_cndmask_b32_e64 v22, v34, v30, s[12:13]
	v_cndmask_b32_e64 v25, v37, v33, s[14:15]
	v_cndmask_b32_e64 v24, v36, v32, s[16:17]
	v_pk_mul_f32 v[18:19], v[18:19], s[54:55] op_sel_hi:[1,0]
	v_pk_mul_f32 v[20:21], v[20:21], s[54:55] op_sel_hi:[1,0]
	v_pk_mul_f32 v[22:23], v[22:23], s[54:55] op_sel_hi:[1,0]
	v_pk_mul_f32 v[24:25], v[24:25], s[54:55] op_sel_hi:[1,0]
	v_cvt_pk_bf16_f32 v18, v18, v19
	v_cvt_pk_bf16_f32 v19, v20, v21
	v_cvt_pk_bf16_f32 v20, v22, v23
	v_cvt_pk_bf16_f32 v21, v24, v25
	s_cmpk_lt_i32 s37, 0x100
	global_store_dwordx4 v[10:11], v[18:21], off
	v_lshl_add_u64 v[10:11], v[10:11], 0, s[34:35]
	s_cbranch_scc1 .LBB0_277
.LBB0_278:
	s_branch .Lmoe_site_T0
.Lmoe_ret_T0:
	s_add_u32 s0, s86, 0x4000
	s_getreg_b32 s2, hwreg(HW_REG_XCC_ID, 0, 4)
	s_waitcnt vmcnt(0)
	v_writelane_b32 v254, s0, 38
	s_addc_u32 s0, s87, 0
	v_writelane_b32 v254, s0, 39
	s_barrier
	s_mov_b64 s[0:1], exec
	v_readlane_b32 s4, v253, 4
	v_readlane_b32 s5, v253, 5
	s_and_b64 s[4:5], s[0:1], s[4:5]
	s_mov_b64 exec, s[4:5]
	s_cbranch_execz .LBB0_330
	s_add_i32 s3, 0, 0x24020
	v_mov_b32_e32 v1, s3
	s_waitcnt vmcnt(0) expcnt(0) lgkmcnt(0)
	ds_read_b32 v3, v1
	s_add_i32 s3, 0, 0x24024
	v_mov_b32_e32 v1, s3
	ds_read_b32 v1, v1
	s_and_b32 s33, s2, 15
	s_waitcnt lgkmcnt(1)
	v_cmp_ne_u32_e32 vcc, 0, v3
	s_cbranch_vccnz .LBB0_294
	v_readlane_b32 s4, v253, 0
	v_readlane_b32 s5, v253, 1
	s_load_dwordx2 s[2:3], s[4:5], 0x4
	s_add_u32 s4, s86, 0x4200
	s_addc_u32 s5, s87, 0
	s_add_u32 s6, s86, 0x4400
	s_addc_u32 s7, s87, 0
	s_add_u32 s8, s86, 0x4500
	s_addc_u32 s9, s87, 0
	s_add_u32 s10, s86, 0x4600
	s_addc_u32 s11, s87, 0
	s_add_u32 s12, s86, 0x4700
	s_addc_u32 s13, s87, 0
	s_add_u32 s14, s86, 0x4800
	s_addc_u32 s15, s87, 0
	s_add_u32 s16, s86, 0x4900
	s_addc_u32 s17, s87, 0
	s_add_u32 s18, s86, 0x4a00
	s_addc_u32 s19, s87, 0
	s_add_u32 s20, s86, 0x4b00
	s_addc_u32 s21, s87, 0
	s_add_u32 s22, s86, 0x4c00
	s_addc_u32 s23, s87, 0
	s_add_u32 s24, s86, 0x4d00
	s_addc_u32 s25, s87, 0
	s_add_u32 s26, s86, 0x4e00
	s_addc_u32 s27, s87, 0
	s_add_u32 s28, s86, 0x4f00
	s_addc_u32 s29, s87, 0
	s_add_u32 s30, s86, 0x5000
	s_addc_u32 s31, s87, 0
	s_add_u32 s34, s86, 0x5100
	s_addc_u32 s35, s87, 0
	s_add_u32 s36, s86, 0x5200
	s_addc_u32 s37, s87, 0
	s_waitcnt lgkmcnt(0)
	s_mul_i32 s2, s2, s95
	s_add_u32 s38, s86, 0x5300
	s_mul_i32 s2, s2, s3
	s_addc_u32 s39, s87, 0
	s_mov_b32 s3, 1
	v_mov_b32_e32 v17, 0
	s_branch .LBB0_282

.LBB0_1363:
.LBB0_1365:
.LBB0_1366:
.LBB0_1368:
.LBB0_1370:
.LBB0_1372:
.LBB0_1374:
.LBB0_1378:
.LBB0_1380:
.LBB0_1381:
.LBB0_1383:
.LBB0_1385:
.LBB0_1387:
.LBB0_1388:
.LBB0_1390:
.LBB0_1392:
.LBB0_1393:
.LBB0_1394:
.LBB0_1395:
.LBB0_1397:
.LBB0_1401:
.LBB0_1403:
.LBB0_1404:
.LBB0_1406:
.LBB0_1408:
.LBB0_1410:
.LBB0_1411:
.LBB0_1414:
.LBB0_1418:
.LBB0_1420:
.LBB0_1421:
.LBB0_1423:
.LBB0_1425:
.Lmoe_site_A:
	s_nop 1
	v_writelane_b32 v255, s0, 0
	v_writelane_b32 v255, s1, 1
	v_writelane_b32 v255, s2, 2
	v_writelane_b32 v255, s3, 3
	v_writelane_b32 v255, s4, 4
	v_writelane_b32 v255, s5, 5
	v_writelane_b32 v255, s6, 6
	v_writelane_b32 v255, s7, 7
	v_writelane_b32 v255, s8, 8
	v_writelane_b32 v255, s9, 9
	v_writelane_b32 v255, s10, 10
	v_writelane_b32 v255, s11, 11
	v_writelane_b32 v255, s12, 12
	v_writelane_b32 v255, s13, 13
	v_writelane_b32 v255, s14, 14
	v_writelane_b32 v255, s15, 15
	v_writelane_b32 v255, s16, 16
	v_writelane_b32 v255, s17, 17
	v_writelane_b32 v255, s18, 18
	v_writelane_b32 v255, s19, 19
	v_writelane_b32 v255, s20, 20
	v_writelane_b32 v255, s21, 21
	v_writelane_b32 v255, s22, 22
	v_writelane_b32 v255, s23, 23
	v_writelane_b32 v255, s24, 24
	v_writelane_b32 v255, s25, 25
	v_writelane_b32 v255, s26, 26
	v_writelane_b32 v255, s27, 27
	v_writelane_b32 v255, s28, 28
	v_writelane_b32 v255, s29, 29
	v_writelane_b32 v255, s30, 30
	v_writelane_b32 v255, s31, 31
	v_writelane_b32 v255, s32, 32
	v_writelane_b32 v255, s33, 33
	v_writelane_b32 v255, s34, 34
	v_writelane_b32 v255, s35, 35
	s_movk_i32 s0, 0
	s_movk_i32 s2, 16
	s_mov_b32 s4, 0x7800
	s_mov_b32 s5, 0xc400
	s_mov_b32 s34, 0xd600
	s_branch .Lmoe_p4
.Lmoe_site_B:
	s_nop 1
	v_writelane_b32 v255, s0, 0
	v_writelane_b32 v255, s1, 1
	v_writelane_b32 v255, s2, 2
	v_writelane_b32 v255, s3, 3
	v_writelane_b32 v255, s4, 4
	v_writelane_b32 v255, s5, 5
	v_writelane_b32 v255, s6, 6
	v_writelane_b32 v255, s7, 7
	v_writelane_b32 v255, s8, 8
	v_writelane_b32 v255, s9, 9
	v_writelane_b32 v255, s10, 10
	v_writelane_b32 v255, s11, 11
	v_writelane_b32 v255, s12, 12
	v_writelane_b32 v255, s13, 13
	v_writelane_b32 v255, s14, 14
	v_writelane_b32 v255, s15, 15
	v_writelane_b32 v255, s16, 16
	v_writelane_b32 v255, s17, 17
	v_writelane_b32 v255, s18, 18
	v_writelane_b32 v255, s19, 19
	v_writelane_b32 v255, s20, 20
	v_writelane_b32 v255, s21, 21
	v_writelane_b32 v255, s22, 22
	v_writelane_b32 v255, s23, 23
	v_writelane_b32 v255, s24, 24
	v_writelane_b32 v255, s25, 25
	v_writelane_b32 v255, s26, 26
	v_writelane_b32 v255, s27, 27
	v_writelane_b32 v255, s28, 28
	v_writelane_b32 v255, s29, 29
	v_writelane_b32 v255, s30, 30
	v_writelane_b32 v255, s31, 31
	v_writelane_b32 v255, s32, 32
	v_writelane_b32 v255, s33, 33
	v_writelane_b32 v255, s34, 34
	v_writelane_b32 v255, s35, 35
	s_movk_i32 s0, 1
	s_movk_i32 s2, 8
	s_mov_b32 s4, 0x800
	s_mov_b32 s5, 0x5000
	s_mov_b32 s34, 0x6000
	s_branch .Lmoe_p4

.Lmoe_site_E:
	s_nop 1
	v_writelane_b32 v255, s0, 0
	v_writelane_b32 v255, s1, 1
	v_writelane_b32 v255, s2, 2
	v_writelane_b32 v255, s3, 3
	v_writelane_b32 v255, s4, 4
	v_writelane_b32 v255, s5, 5
	v_writelane_b32 v255, s6, 6
	v_writelane_b32 v255, s7, 7
	v_writelane_b32 v255, s8, 8
	v_writelane_b32 v255, s9, 9
	v_writelane_b32 v255, s10, 10
	v_writelane_b32 v255, s11, 11
	v_writelane_b32 v255, s12, 12
	v_writelane_b32 v255, s13, 13
	v_writelane_b32 v255, s14, 14
	v_writelane_b32 v255, s15, 15
	v_writelane_b32 v255, s16, 16
	v_writelane_b32 v255, s17, 17
	v_writelane_b32 v255, s18, 18
	v_writelane_b32 v255, s19, 19
	v_writelane_b32 v255, s20, 20
	v_writelane_b32 v255, s21, 21
	v_writelane_b32 v255, s22, 22
	v_writelane_b32 v255, s23, 23
	v_writelane_b32 v255, s24, 24
	v_writelane_b32 v255, s25, 25
	v_writelane_b32 v255, s26, 26
	v_writelane_b32 v255, s27, 27
	v_writelane_b32 v255, s28, 28
	v_writelane_b32 v255, s29, 29
	v_writelane_b32 v255, s30, 30
	v_writelane_b32 v255, s31, 31
	v_writelane_b32 v255, s32, 32
	v_writelane_b32 v255, s33, 33
	v_writelane_b32 v255, s34, 34
	v_writelane_b32 v255, s35, 35
	s_movk_i32 s0, 3
	s_movk_i32 s2, 24
	s_mov_b32 s4, 0xfc00
	s_mov_b32 s5, 0x14800
	s_mov_b32 s34, 0x15a00
	s_branch .Lmoe_p4
.Lmoe_site_T1:
	s_nop 1
	v_writelane_b32 v255, s0, 0
	v_writelane_b32 v255, s1, 1
	v_writelane_b32 v255, s2, 2
	v_writelane_b32 v255, s3, 3
	v_writelane_b32 v255, s4, 4
	v_writelane_b32 v255, s5, 5
	v_writelane_b32 v255, s6, 6
	v_writelane_b32 v255, s7, 7
	v_writelane_b32 v255, s8, 8
	v_writelane_b32 v255, s9, 9
	v_writelane_b32 v255, s10, 10
	v_writelane_b32 v255, s11, 11
	v_writelane_b32 v255, s12, 12
	v_writelane_b32 v255, s13, 13
	v_writelane_b32 v255, s14, 14
	v_writelane_b32 v255, s15, 15
	v_writelane_b32 v255, s16, 16
	v_writelane_b32 v255, s17, 17
	v_writelane_b32 v255, s18, 18
	v_writelane_b32 v255, s19, 19
	v_writelane_b32 v255, s20, 20
	v_writelane_b32 v255, s21, 21
	v_writelane_b32 v255, s22, 22
	v_writelane_b32 v255, s23, 23
	v_writelane_b32 v255, s24, 24
	v_writelane_b32 v255, s25, 25
	v_writelane_b32 v255, s26, 26
	v_writelane_b32 v255, s27, 27
	v_writelane_b32 v255, s28, 28
	v_writelane_b32 v255, s29, 29
	v_writelane_b32 v255, s30, 30
	v_writelane_b32 v255, s31, 31
	v_writelane_b32 v255, s32, 32
	v_writelane_b32 v255, s33, 33
	v_writelane_b32 v255, s34, 34
	v_writelane_b32 v255, s35, 35
	s_movk_i32 s0, 4
	v_readlane_b32 s20, v252, 32
	s_nop 3
	s_cmp_eq_u32 s20, 0
	s_cbranch_scc1 .Lmoe_T1_l1
	s_movk_i32 s2, 32
	s_movk_i32 s26, 1792
	s_mov_b32 s27, 0x2800
	s_mov_b32 s28, 0x6000
	s_mov_b32 s29, 0x5000
	s_mov_b32 s32, 0x9c00
	s_mov_b32 s33, 0xe800
	s_mov_b32 s5, 0x4600
	s_mov_b32 s35, 0x0
	s_movk_i32 s34, 10
	s_branch .Lmoe_tail

.Lmoe_site_T3:
	s_nop 1
	v_writelane_b32 v255, s0, 0
	v_writelane_b32 v255, s1, 1
	v_writelane_b32 v255, s2, 2
	v_writelane_b32 v255, s3, 3
	v_writelane_b32 v255, s4, 4
	v_writelane_b32 v255, s5, 5
	v_writelane_b32 v255, s6, 6
	v_writelane_b32 v255, s7, 7
	v_writelane_b32 v255, s8, 8
	v_writelane_b32 v255, s9, 9
	v_writelane_b32 v255, s10, 10
	v_writelane_b32 v255, s11, 11
	v_writelane_b32 v255, s12, 12
	v_writelane_b32 v255, s13, 13
	v_writelane_b32 v255, s14, 14
	v_writelane_b32 v255, s15, 15
	v_writelane_b32 v255, s16, 16
	v_writelane_b32 v255, s17, 17
	v_writelane_b32 v255, s18, 18
	v_writelane_b32 v255, s19, 19
	v_writelane_b32 v255, s20, 20
	v_writelane_b32 v255, s21, 21
	v_writelane_b32 v255, s22, 22
	v_writelane_b32 v255, s23, 23
	v_writelane_b32 v255, s24, 24
	v_writelane_b32 v255, s25, 25
	v_writelane_b32 v255, s26, 26
	v_writelane_b32 v255, s27, 27
	v_writelane_b32 v255, s28, 28
	v_writelane_b32 v255, s29, 29
	v_writelane_b32 v255, s30, 30
	v_writelane_b32 v255, s31, 31
	v_writelane_b32 v255, s32, 32
	v_writelane_b32 v255, s33, 33
	v_writelane_b32 v255, s34, 34
	v_writelane_b32 v255, s35, 35
	s_movk_i32 s0, 6
	v_readlane_b32 s20, v252, 32
	s_nop 3
	s_cmp_eq_u32 s20, 0
	s_cbranch_scc1 .Lmoe_T3_l1
	s_movk_i32 s2, 128
	s_movk_i32 s26, 1024
	s_mov_b32 s27, 0x2800
	s_mov_b32 s28, 0x6000
	s_mov_b32 s29, 0x5000
	s_mov_b32 s32, 0x9c00
	s_mov_b32 s33, 0xe800
	s_mov_b32 s5, 0x6600
	s_mov_b32 s35, 0x4600
	s_movk_i32 s34, 8
	s_branch .Lmoe_tail

.Lmoe_site_T0:
	s_nop 1
	v_writelane_b32 v255, s0, 0
	v_writelane_b32 v255, s1, 1
	v_writelane_b32 v255, s2, 2
	v_writelane_b32 v255, s3, 3
	v_writelane_b32 v255, s4, 4
	v_writelane_b32 v255, s5, 5
	v_writelane_b32 v255, s6, 6
	v_writelane_b32 v255, s7, 7
	v_writelane_b32 v255, s8, 8
	v_writelane_b32 v255, s9, 9
	v_writelane_b32 v255, s10, 10
	v_writelane_b32 v255, s11, 11
	v_writelane_b32 v255, s12, 12
	v_writelane_b32 v255, s13, 13
	v_writelane_b32 v255, s14, 14
	v_writelane_b32 v255, s15, 15
	v_writelane_b32 v255, s16, 16
	v_writelane_b32 v255, s17, 17
	v_writelane_b32 v255, s18, 18
	v_writelane_b32 v255, s19, 19
	v_writelane_b32 v255, s20, 20
	v_writelane_b32 v255, s21, 21
	v_writelane_b32 v255, s22, 22
	v_writelane_b32 v255, s23, 23
	v_writelane_b32 v255, s24, 24
	v_writelane_b32 v255, s25, 25
	v_writelane_b32 v255, s26, 26
	v_writelane_b32 v255, s27, 27
	v_writelane_b32 v255, s28, 28
	v_writelane_b32 v255, s29, 29
	v_writelane_b32 v255, s30, 30
	v_writelane_b32 v255, s31, 31
	v_writelane_b32 v255, s32, 32
	v_writelane_b32 v255, s33, 33
	v_writelane_b32 v255, s34, 34
	v_writelane_b32 v255, s35, 35
	s_movk_i32 s0, 7
	s_mov_b64 s[30:31], exec
	s_mov_b64 exec, -1
	v_mov_b32_e32 v174, v75
	s_mov_b64 exec, s[30:31]
	s_movk_i32 s2, 96
	s_movk_i32 s26, 1280
	s_mov_b32 s27, 0x2800
	s_mov_b32 s28, 0x6000
	s_mov_b32 s29, 0x5000
	s_mov_b32 s32, 0x9c00
	s_mov_b32 s33, 0xe800
	s_mov_b32 s5, 0x9800
	s_mov_b32 s35, 0x6600
	s_movk_i32 s34, 10
	s_branch .Lmoe_tail

.Lmoe_exit:
	s_waitcnt vmcnt(0) lgkmcnt(0)
	s_mov_b64 exec, s[30:31]
	s_cmp_eq_u32 s0, 0
	s_cbranch_scc1 .Lmoe_tail_A
	s_cmp_eq_u32 s0, 1
	s_cbranch_scc1 .Lmoe_tail_B
	s_cmp_eq_u32 s0, 2
	s_cbranch_scc1 .Lmoe_tail_D
	s_cmp_eq_u32 s0, 3
	s_cbranch_scc1 .Lmoe_tail_E
	s_cmp_eq_u32 s0, 4
	s_cbranch_scc1 .Lmoe_tail_T1
	s_cmp_eq_u32 s0, 5
	s_cbranch_scc1 .Lmoe_tail_T2
	s_cmp_eq_u32 s0, 6
	s_cbranch_scc1 .Lmoe_tail_T3
.Lmoe_tail_T0:
	s_mov_b64 s[30:31], exec
	s_mov_b64 exec, -1
	v_mov_b32_e32 v75, v174
	s_mov_b64 exec, s[30:31]
	v_readlane_b32 s0, v255, 0
	v_readlane_b32 s1, v255, 1
	v_readlane_b32 s2, v255, 2
	v_readlane_b32 s3, v255, 3
	v_readlane_b32 s4, v255, 4
	v_readlane_b32 s5, v255, 5
	v_readlane_b32 s6, v255, 6
	v_readlane_b32 s7, v255, 7
	v_readlane_b32 s8, v255, 8
	v_readlane_b32 s9, v255, 9
	v_readlane_b32 s10, v255, 10
	v_readlane_b32 s11, v255, 11
	v_readlane_b32 s12, v255, 12
	v_readlane_b32 s13, v255, 13
	v_readlane_b32 s14, v255, 14
	v_readlane_b32 s15, v255, 15
	v_readlane_b32 s16, v255, 16
	v_readlane_b32 s17, v255, 17
	v_readlane_b32 s18, v255, 18
	v_readlane_b32 s19, v255, 19
	v_readlane_b32 s20, v255, 20
	v_readlane_b32 s21, v255, 21
	v_readlane_b32 s22, v255, 22
	v_readlane_b32 s23, v255, 23
	v_readlane_b32 s24, v255, 24
	v_readlane_b32 s25, v255, 25
	v_readlane_b32 s26, v255, 26
	v_readlane_b32 s27, v255, 27
	v_readlane_b32 s28, v255, 28
	v_readlane_b32 s29, v255, 29
	v_readlane_b32 s30, v255, 30
	v_readlane_b32 s31, v255, 31
	v_readlane_b32 s32, v255, 32
	v_readlane_b32 s33, v255, 33
	v_readlane_b32 s34, v255, 34
	v_readlane_b32 s35, v255, 35
	s_nop 3
	s_branch .Lmoe_ret_T0
